# prep gate blocks: x-row loads marked nt (x is read exactly once now)
# speedup vs baseline: 1.0252x; 1.0196x over previous
.LBB13_3:
	s_cmpk_lt_i32 s2, 0x100
	v_lshrrev_b32_e32 v1, 6, v0
	v_and_b32_e32 v36, 63, v0
	s_cbranch_scc0 .LBB13_5
	v_bfe_u32 v13, v0, 4, 2
	v_and_b32_e32 v12, 15, v0
	s_lshl_b32 s22, s2, 4
	v_lshlrev_b32_e32 v2, 3, v13
	v_lshl_or_b32 v14, v1, 8, v2
	v_or_b32_e32 v2, s22, v12
	s_load_dwordx8 s[4:11], s[0:1], 0x30
	s_load_dwordx2 s[26:27], s[0:1], 0x60
	v_ashrrev_i32_e32 v3, 31, v2
	v_lshlrev_b64 v[2:3], 12, v[2:3]
	s_waitcnt lgkmcnt(0)
	v_lshl_add_u64 v[2:3], s[20:21], 0, v[2:3]
	v_lshlrev_b32_e32 v18, 2, v14
	v_mov_b32_e32 v19, 0
	v_lshl_or_b32 v14, v14, 4, v12
	v_lshl_add_u64 v[10:11], v[2:3], 0, v[18:19]
	v_subrev_u32_e32 v108, s20, v10
	v_lshrrev_b32_e32 v108, 1, v108
	global_load_dwordx4 v[116:119], v[10:11], off offset:528 nt
	global_load_dwordx4 v[112:115], v[10:11], off offset:512 nt
	global_load_dwordx4 v[124:127], v[10:11], off offset:656 nt
	global_load_dwordx4 v[120:123], v[10:11], off offset:640 nt
	global_load_dwordx4 v[132:135], v[10:11], off offset:784 nt
	global_load_dwordx4 v[128:131], v[10:11], off offset:768 nt
	global_load_dwordx4 v[140:143], v[10:11], off offset:912 nt
	global_load_dwordx4 v[136:139], v[10:11], off offset:896 nt
	global_load_dwordx4 v[148:151], v[10:11], off offset:400 nt
	global_load_dwordx4 v[144:147], v[10:11], off offset:384 nt
	v_or_b32_e32 v18, 0x200, v14
	v_lshlrev_b64 v[16:17], 2, v[18:19]
	v_lshlrev_b32_e32 v15, 2, v14
	v_lshl_add_u64 v[28:29], s[4:5], 0, v[16:17]
	v_lshl_add_u64 v[16:17], s[10:11], 0, v[16:17]
	v_or_b32_e32 v18, 0x400, v14
	global_load_dwordx4 v[2:5], v[10:11], off offset:16 nt
	global_load_dwordx4 v[6:9], v[10:11], off nt
	global_load_dword v37, v15, s[4:5]
	global_load_dword v48, v15, s[10:11]
	global_load_dword v49, v15, s[4:5] offset:64
	global_load_dword v50, v15, s[10:11] offset:64
	global_load_dword v51, v15, s[4:5] offset:128
	global_load_dword v52, v15, s[10:11] offset:128
	global_load_dword v53, v15, s[4:5] offset:192
	global_load_dword v54, v15, s[10:11] offset:192
	global_load_dword v55, v15, s[4:5] offset:256
	global_load_dword v56, v15, s[10:11] offset:256
	global_load_dword v57, v15, s[4:5] offset:320
	global_load_dword v58, v15, s[10:11] offset:320
	global_load_dword v59, v15, s[4:5] offset:384
	global_load_dword v60, v15, s[10:11] offset:384
	global_load_dword v61, v15, s[4:5] offset:448
	global_load_dword v62, v15, s[10:11] offset:448
	global_load_dwordx4 v[20:23], v[10:11], off offset:144 nt
	global_load_dwordx4 v[24:27], v[10:11], off offset:128 nt
	global_load_dword v63, v[28:29], off
	global_load_dword v64, v[16:17], off
	global_load_dword v65, v15, s[4:5] offset:2112
	global_load_dword v66, v15, s[10:11] offset:2112
	global_load_dword v67, v15, s[4:5] offset:2176
	global_load_dword v68, v15, s[10:11] offset:2176
	global_load_dword v69, v15, s[4:5] offset:2240
	global_load_dword v70, v15, s[10:11] offset:2240
	global_load_dword v71, v15, s[4:5] offset:2304
	global_load_dword v72, v15, s[10:11] offset:2304
	global_load_dword v73, v15, s[4:5] offset:2368
	global_load_dword v74, v15, s[10:11] offset:2368
	global_load_dword v75, v15, s[4:5] offset:2432
	global_load_dword v76, v15, s[10:11] offset:2432
	global_load_dword v77, v15, s[4:5] offset:2496
	global_load_dword v78, v15, s[10:11] offset:2496
	s_nop 0
	global_load_dwordx4 v[28:31], v[10:11], off offset:272 nt
	global_load_dwordx4 v[32:35], v[10:11], off offset:256 nt
	v_lshlrev_b64 v[16:17], 2, v[18:19]
	v_lshl_add_u64 v[38:39], s[4:5], 0, v[16:17]
	v_lshl_add_u64 v[16:17], s[10:11], 0, v[16:17]
	v_or_b32_e32 v18, 0x410, v14
	global_load_dword v79, v[16:17], off
	v_lshlrev_b64 v[16:17], 2, v[18:19]
	global_load_dword v15, v[38:39], off
	v_lshl_add_u64 v[38:39], s[4:5], 0, v[16:17]
	v_lshl_add_u64 v[16:17], s[10:11], 0, v[16:17]
	v_or_b32_e32 v18, 0x420, v14
	global_load_dword v81, v[16:17], off
	v_lshlrev_b64 v[16:17], 2, v[18:19]
	global_load_dword v80, v[38:39], off
	v_lshl_add_u64 v[38:39], s[4:5], 0, v[16:17]
	v_lshl_add_u64 v[16:17], s[10:11], 0, v[16:17]
	v_or_b32_e32 v18, 0x430, v14
	global_load_dword v83, v[16:17], off
	v_lshlrev_b64 v[16:17], 2, v[18:19]
	global_load_dword v82, v[38:39], off
	v_lshl_add_u64 v[38:39], s[4:5], 0, v[16:17]
	v_lshl_add_u64 v[16:17], s[10:11], 0, v[16:17]
	v_or_b32_e32 v18, 0x440, v14
	global_load_dword v85, v[16:17], off
	v_lshlrev_b64 v[16:17], 2, v[18:19]
	global_load_dword v84, v[38:39], off
	v_lshl_add_u64 v[38:39], s[4:5], 0, v[16:17]
	v_lshl_add_u64 v[16:17], s[10:11], 0, v[16:17]
	v_or_b32_e32 v18, 0x450, v14
	global_load_dword v87, v[16:17], off
	v_lshlrev_b64 v[16:17], 2, v[18:19]
	global_load_dword v86, v[38:39], off
	v_lshl_add_u64 v[38:39], s[4:5], 0, v[16:17]
	v_lshl_add_u64 v[16:17], s[10:11], 0, v[16:17]
	v_or_b32_e32 v18, 0x460, v14
	global_load_dword v89, v[16:17], off
	v_lshlrev_b64 v[16:17], 2, v[18:19]
	global_load_dword v88, v[38:39], off
	v_lshl_add_u64 v[38:39], s[4:5], 0, v[16:17]
	v_lshl_add_u64 v[16:17], s[10:11], 0, v[16:17]
	v_or_b32_e32 v18, 0x470, v14
	global_load_dword v91, v[16:17], off
	v_lshlrev_b64 v[16:17], 2, v[18:19]
	global_load_dword v90, v[38:39], off
	v_lshl_add_u64 v[38:39], s[4:5], 0, v[16:17]
	v_lshl_add_u64 v[16:17], s[10:11], 0, v[16:17]
	v_or_b32_e32 v18, 0x600, v14
	global_load_dword v92, v[38:39], off
	global_load_dword v93, v[16:17], off
	s_nop 0
	v_lshlrev_b64 v[16:17], 2, v[18:19]
	v_lshl_add_u64 v[46:47], s[4:5], 0, v[16:17]
	v_lshl_add_u64 v[16:17], s[10:11], 0, v[16:17]
	v_or_b32_e32 v18, 0x610, v14
	global_load_dword v95, v[16:17], off
	v_lshlrev_b64 v[16:17], 2, v[18:19]
	global_load_dword v94, v[46:47], off
	v_lshl_add_u64 v[46:47], s[4:5], 0, v[16:17]
	v_lshl_add_u64 v[16:17], s[10:11], 0, v[16:17]
	v_or_b32_e32 v18, 0x620, v14
	global_load_dword v97, v[16:17], off
	v_lshlrev_b64 v[16:17], 2, v[18:19]
	global_load_dword v96, v[46:47], off
	v_lshl_add_u64 v[46:47], s[4:5], 0, v[16:17]
	v_lshl_add_u64 v[16:17], s[10:11], 0, v[16:17]
	v_or_b32_e32 v18, 0x630, v14
	global_load_dword v99, v[16:17], off
	v_lshlrev_b64 v[16:17], 2, v[18:19]
	global_load_dword v98, v[46:47], off
	v_lshl_add_u64 v[46:47], s[4:5], 0, v[16:17]
	v_lshl_add_u64 v[16:17], s[10:11], 0, v[16:17]
	v_or_b32_e32 v18, 0x640, v14
	global_load_dword v101, v[16:17], off
	v_lshlrev_b64 v[16:17], 2, v[18:19]
	global_load_dword v100, v[46:47], off
	v_lshl_add_u64 v[46:47], s[4:5], 0, v[16:17]
	v_lshl_add_u64 v[16:17], s[10:11], 0, v[16:17]
	v_or_b32_e32 v18, 0x650, v14
	global_load_dword v103, v[16:17], off
	v_lshlrev_b64 v[16:17], 2, v[18:19]
	global_load_dword v102, v[46:47], off
	v_lshl_add_u64 v[46:47], s[4:5], 0, v[16:17]
	v_lshl_add_u64 v[16:17], s[10:11], 0, v[16:17]
	v_or_b32_e32 v18, 0x660, v14
	global_load_dword v105, v[16:17], off
	v_lshlrev_b64 v[16:17], 2, v[18:19]
	global_load_dword v104, v[46:47], off
	v_lshl_add_u64 v[46:47], s[4:5], 0, v[16:17]
	v_lshl_add_u64 v[16:17], s[10:11], 0, v[16:17]
	v_or_b32_e32 v18, 0x670, v14
	global_load_dword v107, v[16:17], off
	v_lshlrev_b64 v[16:17], 2, v[18:19]
	global_load_dword v106, v[46:47], off
	v_lshl_add_u64 v[46:47], s[4:5], 0, v[16:17]
	v_lshl_add_u64 v[16:17], s[10:11], 0, v[16:17]
	global_load_dword v18, v[46:47], off
	s_mov_b32 s23, 0
	global_load_dword v16, v[16:17], off
	s_load_dwordx2 s[24:25], s[0:1], 0x88
	s_load_dwordx4 s[12:15], s[0:1], 0x78
	s_load_dwordx4 s[16:19], s[0:1], 0x50
	s_waitcnt vmcnt(60)
	v_cvt_pk_f16_f32 v6, v6, v7
	v_cvt_pk_f16_f32 v7, v8, v9
	v_cvt_pk_f16_f32 v8, v2, v3
	v_cvt_pk_f16_f32 v9, v4, v5
	v_cvt_pk_f16_f32 v2, v37, v49
	v_cvt_pk_f16_f32 v3, v51, v53
	s_waitcnt vmcnt(57)
	v_cvt_pk_f16_f32 v4, v55, v57
	s_waitcnt vmcnt(53)
	v_cvt_pk_f16_f32 v5, v59, v61
	v_cvt_pk_f16_f32 v46, v48, v50
	v_cvt_pk_f16_f32 v47, v52, v54
	v_mfma_f32_16x16x32_f16 a[0:3], v[6:9], v[2:5], 0
	global_store_dwordx4 v108, v[6:9], s[26:27] offset:0
	v_cvt_pk_f16_f32 v48, v56, v58
	s_waitcnt vmcnt(53)
	v_cvt_pk_f16_f32 v49, v60, v62
	s_waitcnt vmcnt(51)
	v_cvt_pk_f16_f32 v2, v24, v25
	v_cvt_pk_f16_f32 v3, v26, v27
	v_cvt_pk_f16_f32 v4, v20, v21
	v_cvt_pk_f16_f32 v5, v22, v23
	v_mfma_f32_16x16x32_f16 a[4:7], v[6:9], v[46:49], 0
	s_waitcnt vmcnt(48)
	v_cvt_pk_f16_f32 v6, v63, v65
	s_waitcnt vmcnt(47)
	v_cvt_pk_f16_f32 v20, v64, v66
	s_waitcnt vmcnt(44)
	v_cvt_pk_f16_f32 v7, v67, v69
	s_waitcnt vmcnt(40)
	v_cvt_pk_f16_f32 v8, v71, v73
	s_waitcnt vmcnt(36)
	v_cvt_pk_f16_f32 v9, v75, v77
	v_cvt_pk_f16_f32 v21, v68, v70
	v_cvt_pk_f16_f32 v22, v72, v74
	s_waitcnt vmcnt(35)
	v_cvt_pk_f16_f32 v23, v76, v78
	v_mfma_f32_16x16x32_f16 a[0:3], v[2:5], v[6:9], a[0:3]
	global_store_dwordx4 v108, v[2:5], s[26:27] offset:64
	s_waitcnt vmcnt(30)
	v_cvt_pk_f16_f32 v6, v15, v80
	s_waitcnt vmcnt(26)
	v_cvt_pk_f16_f32 v7, v82, v84
	s_waitcnt vmcnt(22)
	v_cvt_pk_f16_f32 v8, v86, v88
	v_mfma_f32_16x16x32_f16 a[4:7], v[2:5], v[20:23], a[4:7]
	v_cvt_pk_f16_f32 v2, v32, v33
	v_cvt_pk_f16_f32 v3, v34, v35
	v_cvt_pk_f16_f32 v4, v28, v29
	v_cvt_pk_f16_f32 v5, v30, v31
	v_cvt_pk_f16_f32 v20, v79, v81
	s_waitcnt vmcnt(19)
	v_cvt_pk_f16_f32 v9, v90, v92
	v_cvt_pk_f16_f32 v21, v83, v85
	v_cvt_pk_f16_f32 v22, v87, v89
	s_waitcnt vmcnt(18)
	v_cvt_pk_f16_f32 v23, v91, v93
	v_mfma_f32_16x16x32_f16 a[0:3], v[2:5], v[6:9], a[0:3]
	global_store_dwordx4 v108, v[2:5], s[26:27] offset:128
	s_waitcnt vmcnt(15)
	v_cvt_pk_f16_f32 v6, v94, v96
	s_waitcnt vmcnt(11)
	v_cvt_pk_f16_f32 v7, v98, v100
	s_waitcnt vmcnt(7)
	v_cvt_pk_f16_f32 v8, v102, v104
	v_mfma_f32_16x16x32_f16 a[8:11], v[2:5], v[20:23], a[4:7]
	v_cvt_pk_f16_f32 v2, v144, v145
	v_cvt_pk_f16_f32 v3, v146, v147
	v_cvt_pk_f16_f32 v4, v148, v149
	v_cvt_pk_f16_f32 v5, v150, v151
	v_cvt_pk_f16_f32 v20, v95, v97
	s_waitcnt vmcnt(4)
	v_cvt_pk_f16_f32 v9, v106, v18
	v_cvt_pk_f16_f32 v21, v99, v101
	v_cvt_pk_f16_f32 v22, v103, v105
	s_waitcnt vmcnt(3)
	v_cvt_pk_f16_f32 v23, v107, v16
	v_mfma_f32_16x16x32_f16 a[4:7], v[2:5], v[6:9], a[0:3]
	global_store_dwordx4 v108, v[2:5], s[26:27] offset:192
	s_nop 0
	v_mfma_f32_16x16x32_f16 a[0:3], v[2:5], v[20:23], a[8:11]
	v_or_b32_e32 v18, 0x800, v14
	v_lshlrev_b64 v[16:17], 2, v[18:19]
	v_lshl_add_u64 v[20:21], s[4:5], 0, v[16:17]
	v_lshl_add_u64 v[16:17], s[10:11], 0, v[16:17]
	v_or_b32_e32 v18, 0x810, v14
	global_load_dword v46, v[16:17], off
	v_lshlrev_b64 v[16:17], 2, v[18:19]
	global_load_dword v37, v[20:21], off
	v_lshl_add_u64 v[20:21], s[4:5], 0, v[16:17]
	v_lshl_add_u64 v[16:17], s[10:11], 0, v[16:17]
	v_or_b32_e32 v18, 0x820, v14
	global_load_dword v48, v[16:17], off
	v_lshlrev_b64 v[16:17], 2, v[18:19]
	global_load_dword v47, v[20:21], off
	v_lshl_add_u64 v[20:21], s[4:5], 0, v[16:17]
	v_lshl_add_u64 v[16:17], s[10:11], 0, v[16:17]
	v_or_b32_e32 v18, 0x830, v14
	global_load_dword v50, v[16:17], off
	v_lshlrev_b64 v[16:17], 2, v[18:19]
	global_load_dword v49, v[20:21], off
	v_lshl_add_u64 v[20:21], s[4:5], 0, v[16:17]
	v_lshl_add_u64 v[16:17], s[10:11], 0, v[16:17]
	v_or_b32_e32 v18, 0x840, v14
	global_load_dword v52, v[16:17], off
	v_lshlrev_b64 v[16:17], 2, v[18:19]
	global_load_dword v51, v[20:21], off
	v_lshl_add_u64 v[20:21], s[4:5], 0, v[16:17]
	v_lshl_add_u64 v[16:17], s[10:11], 0, v[16:17]
	v_or_b32_e32 v18, 0x850, v14
	global_load_dword v54, v[16:17], off
	v_lshlrev_b64 v[16:17], 2, v[18:19]
	global_load_dword v53, v[20:21], off
	v_lshl_add_u64 v[20:21], s[4:5], 0, v[16:17]
	v_lshl_add_u64 v[16:17], s[10:11], 0, v[16:17]
	v_or_b32_e32 v18, 0x860, v14
	global_load_dword v56, v[16:17], off
	v_lshlrev_b64 v[16:17], 2, v[18:19]
	global_load_dword v55, v[20:21], off
	v_lshl_add_u64 v[20:21], s[4:5], 0, v[16:17]
	v_lshl_add_u64 v[16:17], s[10:11], 0, v[16:17]
	v_or_b32_e32 v18, 0x870, v14
	global_load_dword v58, v[16:17], off
	v_lshlrev_b64 v[16:17], 2, v[18:19]
	global_load_dword v57, v[20:21], off
	v_lshl_add_u64 v[20:21], s[4:5], 0, v[16:17]
	v_lshl_add_u64 v[16:17], s[10:11], 0, v[16:17]
	v_or_b32_e32 v18, 0xa00, v14
	global_load_dword v59, v[20:21], off
	global_load_dword v60, v[16:17], off
	s_nop 0
	v_lshlrev_b64 v[16:17], 2, v[18:19]
	v_lshl_add_u64 v[28:29], s[4:5], 0, v[16:17]
	v_lshl_add_u64 v[16:17], s[10:11], 0, v[16:17]
	v_or_b32_e32 v18, 0xa10, v14
	global_load_dword v62, v[16:17], off
	v_lshlrev_b64 v[16:17], 2, v[18:19]
	global_load_dword v61, v[28:29], off
	v_lshl_add_u64 v[28:29], s[4:5], 0, v[16:17]
	v_lshl_add_u64 v[16:17], s[10:11], 0, v[16:17]
	v_or_b32_e32 v18, 0xa20, v14
	global_load_dword v64, v[16:17], off
	v_lshlrev_b64 v[16:17], 2, v[18:19]
	global_load_dword v63, v[28:29], off
	v_lshl_add_u64 v[28:29], s[4:5], 0, v[16:17]
	v_lshl_add_u64 v[16:17], s[10:11], 0, v[16:17]
	v_or_b32_e32 v18, 0xa30, v14
	global_load_dword v66, v[16:17], off
	v_lshlrev_b64 v[16:17], 2, v[18:19]
	global_load_dword v65, v[28:29], off
	v_lshl_add_u64 v[28:29], s[4:5], 0, v[16:17]
	v_lshl_add_u64 v[16:17], s[10:11], 0, v[16:17]
	v_or_b32_e32 v18, 0xa40, v14
	global_load_dword v68, v[16:17], off
	v_lshlrev_b64 v[16:17], 2, v[18:19]
	global_load_dword v67, v[28:29], off
	v_lshl_add_u64 v[28:29], s[4:5], 0, v[16:17]
	v_lshl_add_u64 v[16:17], s[10:11], 0, v[16:17]
	v_or_b32_e32 v18, 0xa50, v14
	global_load_dword v70, v[16:17], off
	v_lshlrev_b64 v[16:17], 2, v[18:19]
	global_load_dword v69, v[28:29], off
	v_lshl_add_u64 v[28:29], s[4:5], 0, v[16:17]
	v_lshl_add_u64 v[16:17], s[10:11], 0, v[16:17]
	v_or_b32_e32 v18, 0xa60, v14
	global_load_dword v72, v[16:17], off
	v_lshlrev_b64 v[16:17], 2, v[18:19]
	global_load_dword v71, v[28:29], off
	v_lshl_add_u64 v[28:29], s[4:5], 0, v[16:17]
	v_lshl_add_u64 v[16:17], s[10:11], 0, v[16:17]
	v_or_b32_e32 v18, 0xa70, v14
	global_load_dword v74, v[16:17], off
	v_lshlrev_b64 v[16:17], 2, v[18:19]
	global_load_dword v73, v[28:29], off
	v_lshl_add_u64 v[28:29], s[4:5], 0, v[16:17]
	v_lshl_add_u64 v[16:17], s[10:11], 0, v[16:17]
	v_or_b32_e32 v18, 0xc00, v14
	global_load_dword v75, v[28:29], off
	global_load_dword v76, v[16:17], off
	s_nop 0
	v_lshlrev_b64 v[16:17], 2, v[18:19]
	v_lshl_add_u64 v[38:39], s[4:5], 0, v[16:17]
	v_lshl_add_u64 v[16:17], s[10:11], 0, v[16:17]
	v_or_b32_e32 v18, 0xc10, v14
	global_load_dword v78, v[16:17], off
	v_lshlrev_b64 v[16:17], 2, v[18:19]
	global_load_dword v77, v[38:39], off
	v_lshl_add_u64 v[38:39], s[4:5], 0, v[16:17]
	v_lshl_add_u64 v[16:17], s[10:11], 0, v[16:17]
	v_or_b32_e32 v18, 0xc20, v14
	global_load_dword v80, v[16:17], off
	v_lshlrev_b64 v[16:17], 2, v[18:19]
	global_load_dword v79, v[38:39], off
	v_lshl_add_u64 v[38:39], s[4:5], 0, v[16:17]
	v_lshl_add_u64 v[16:17], s[10:11], 0, v[16:17]
	v_or_b32_e32 v18, 0xc30, v14
	global_load_dword v82, v[16:17], off
	v_lshlrev_b64 v[16:17], 2, v[18:19]
	global_load_dword v81, v[38:39], off
	v_lshl_add_u64 v[38:39], s[4:5], 0, v[16:17]
	v_lshl_add_u64 v[16:17], s[10:11], 0, v[16:17]
	v_or_b32_e32 v18, 0xc40, v14
	global_load_dword v84, v[16:17], off
	v_lshlrev_b64 v[16:17], 2, v[18:19]
	global_load_dword v83, v[38:39], off
	v_lshl_add_u64 v[38:39], s[4:5], 0, v[16:17]
	v_lshl_add_u64 v[16:17], s[10:11], 0, v[16:17]
	v_or_b32_e32 v18, 0xc50, v14
	global_load_dword v86, v[16:17], off
	v_lshlrev_b64 v[16:17], 2, v[18:19]
	global_load_dword v85, v[38:39], off
	v_lshl_add_u64 v[38:39], s[4:5], 0, v[16:17]
	v_lshl_add_u64 v[16:17], s[10:11], 0, v[16:17]
	v_or_b32_e32 v18, 0xc60, v14
	global_load_dword v88, v[16:17], off
	v_lshlrev_b64 v[16:17], 2, v[18:19]
	global_load_dword v87, v[38:39], off
	v_lshl_add_u64 v[38:39], s[4:5], 0, v[16:17]
	v_lshl_add_u64 v[16:17], s[10:11], 0, v[16:17]
	v_or_b32_e32 v18, 0xc70, v14
	global_load_dword v90, v[16:17], off
	v_lshlrev_b64 v[16:17], 2, v[18:19]
	global_load_dword v89, v[38:39], off
	v_lshl_add_u64 v[38:39], s[4:5], 0, v[16:17]
	v_lshl_add_u64 v[16:17], s[10:11], 0, v[16:17]
	v_or_b32_e32 v18, 0xe00, v14
	global_load_dword v91, v[38:39], off
	global_load_dword v92, v[16:17], off
	s_nop 0
	v_lshlrev_b64 v[10:11], 2, v[18:19]
	v_lshl_add_u64 v[16:17], s[4:5], 0, v[10:11]
	v_lshl_add_u64 v[10:11], s[10:11], 0, v[10:11]
	v_or_b32_e32 v18, 0xe10, v14
	global_load_dword v94, v[10:11], off
	v_lshlrev_b64 v[10:11], 2, v[18:19]
	global_load_dword v93, v[16:17], off
	v_lshl_add_u64 v[16:17], s[4:5], 0, v[10:11]
	v_lshl_add_u64 v[10:11], s[10:11], 0, v[10:11]
	v_or_b32_e32 v18, 0xe20, v14
	global_load_dword v96, v[10:11], off
	v_lshlrev_b64 v[10:11], 2, v[18:19]
	global_load_dword v95, v[16:17], off
	v_lshl_add_u64 v[16:17], s[4:5], 0, v[10:11]
	v_lshl_add_u64 v[10:11], s[10:11], 0, v[10:11]
	v_or_b32_e32 v18, 0xe30, v14
	global_load_dword v98, v[10:11], off
	v_lshlrev_b64 v[10:11], 2, v[18:19]
	global_load_dword v97, v[16:17], off
	v_lshl_add_u64 v[16:17], s[4:5], 0, v[10:11]
	v_lshl_add_u64 v[10:11], s[10:11], 0, v[10:11]
	v_or_b32_e32 v18, 0xe40, v14
	global_load_dword v100, v[10:11], off
	v_lshlrev_b64 v[10:11], 2, v[18:19]
	global_load_dword v99, v[16:17], off
	v_lshl_add_u64 v[16:17], s[4:5], 0, v[10:11]
	v_lshl_add_u64 v[10:11], s[10:11], 0, v[10:11]
	v_or_b32_e32 v18, 0xe50, v14
	global_load_dword v102, v[10:11], off
	v_lshlrev_b64 v[10:11], 2, v[18:19]
	global_load_dword v101, v[16:17], off
	v_lshl_add_u64 v[16:17], s[4:5], 0, v[10:11]
	v_lshl_add_u64 v[10:11], s[10:11], 0, v[10:11]
	v_or_b32_e32 v18, 0xe60, v14
	global_load_dword v104, v[10:11], off
	v_lshlrev_b64 v[10:11], 2, v[18:19]
	global_load_dword v103, v[16:17], off
	v_lshl_add_u64 v[16:17], s[4:5], 0, v[10:11]
	v_lshl_add_u64 v[10:11], s[10:11], 0, v[10:11]
	v_or_b32_e32 v18, 0xe70, v14
	global_load_dword v106, v[10:11], off
	v_lshlrev_b64 v[10:11], 2, v[18:19]
	v_lshl_add_u64 v[14:15], s[4:5], 0, v[10:11]
	v_lshl_add_u64 v[10:11], s[10:11], 0, v[10:11]
	global_load_dword v105, v[16:17], off
	global_load_dword v18, v[14:15], off
	s_nop 0
	global_load_dword v10, v[10:11], off
	s_waitcnt vmcnt(56)
	v_cvt_pk_f16_f32 v6, v112, v113
	v_cvt_pk_f16_f32 v7, v114, v115
	v_cvt_pk_f16_f32 v8, v116, v117
	v_cvt_pk_f16_f32 v9, v118, v119
	v_cvt_pk_f16_f32 v2, v37, v47
	v_cvt_pk_f16_f32 v3, v49, v51
	s_waitcnt vmcnt(52)
	v_cvt_pk_f16_f32 v4, v53, v55
	s_waitcnt vmcnt(49)
	v_cvt_pk_f16_f32 v5, v57, v59
	s_waitcnt vmcnt(45)
	v_cvt_pk_f16_f32 v14, v62, v64
	s_waitcnt vmcnt(41)
	v_cvt_pk_f16_f32 v15, v66, v68
	v_mfma_f32_16x16x32_f16 a[4:7], v[6:9], v[2:5], a[4:7]
	global_store_dwordx4 v108, v[6:9], s[26:27] offset:256
	v_cvt_pk_f16_f32 v2, v46, v48
	v_cvt_pk_f16_f32 v3, v50, v52
	v_cvt_pk_f16_f32 v4, v54, v56
	v_cvt_pk_f16_f32 v5, v58, v60
	s_waitcnt vmcnt(38)
	v_cvt_pk_f16_f32 v16, v70, v72
	s_waitcnt vmcnt(33)
	v_cvt_pk_f16_f32 v17, v74, v76
	v_mfma_f32_16x16x32_f16 a[0:3], v[6:9], v[2:5], a[0:3]
	v_cvt_pk_f16_f32 v2, v120, v121
	v_cvt_pk_f16_f32 v3, v122, v123
	v_cvt_pk_f16_f32 v4, v124, v125
	v_cvt_pk_f16_f32 v5, v126, v127
	v_cvt_pk_f16_f32 v6, v61, v63
	v_cvt_pk_f16_f32 v7, v65, v67
	v_cvt_pk_f16_f32 v8, v69, v71
	v_cvt_pk_f16_f32 v9, v73, v75
	v_mfma_f32_16x16x32_f16 a[0:3], v[2:5], v[14:17], a[0:3]
	global_store_dwordx4 v108, v[2:5], s[26:27] offset:320
	s_waitcnt vmcnt(31)
	v_cvt_pk_f16_f32 v14, v78, v80
	s_waitcnt vmcnt(27)
	v_cvt_pk_f16_f32 v15, v82, v84
	s_waitcnt vmcnt(23)
	v_cvt_pk_f16_f32 v16, v86, v88
	v_mfma_f32_16x16x32_f16 a[4:7], v[2:5], v[6:9], a[4:7]
	v_cvt_pk_f16_f32 v2, v128, v129
	v_cvt_pk_f16_f32 v3, v130, v131
	v_cvt_pk_f16_f32 v4, v132, v133
	v_cvt_pk_f16_f32 v5, v134, v135
	v_cvt_pk_f16_f32 v6, v77, v79
	v_cvt_pk_f16_f32 v7, v81, v83
	s_waitcnt vmcnt(22)
	v_cvt_pk_f16_f32 v8, v85, v87
	s_waitcnt vmcnt(19)
	v_cvt_pk_f16_f32 v9, v89, v91
	s_waitcnt vmcnt(18)
	v_cvt_pk_f16_f32 v17, v90, v92
	v_mfma_f32_16x16x32_f16 a[4:7], v[2:5], v[6:9], a[4:7]
	global_store_dwordx4 v108, v[2:5], s[26:27] offset:384
	s_waitcnt vmcnt(15)
	v_cvt_pk_f16_f32 v6, v93, v95
	s_waitcnt vmcnt(11)
	v_cvt_pk_f16_f32 v7, v97, v99
	s_waitcnt vmcnt(7)
	v_cvt_pk_f16_f32 v8, v101, v103
	v_mfma_f32_16x16x32_f16 a[0:3], v[2:5], v[14:17], a[0:3]
	v_cvt_pk_f16_f32 v2, v136, v137
	v_cvt_pk_f16_f32 v3, v138, v139
	v_cvt_pk_f16_f32 v4, v140, v141
	v_cvt_pk_f16_f32 v5, v142, v143
	v_cvt_pk_f16_f32 v14, v94, v96
	s_waitcnt vmcnt(4)
	v_cvt_pk_f16_f32 v9, v105, v18
	v_cvt_pk_f16_f32 v15, v98, v100
	v_cvt_pk_f16_f32 v16, v102, v104
	s_waitcnt vmcnt(3)
	v_cvt_pk_f16_f32 v17, v106, v10
	v_mfma_f32_16x16x32_f16 a[4:7], v[2:5], v[6:9], a[4:7]
	global_store_dwordx4 v108, v[2:5], s[26:27] offset:448
	s_nop 0
	v_mfma_f32_16x16x32_f16 a[0:3], v[2:5], v[14:17], a[0:3]
	v_lshlrev_b32_e32 v2, 11, v1
	v_lshlrev_b32_e32 v3, 2, v12
	v_lshlrev_b32_e32 v4, 8, v13
	v_lshlrev_b32_e32 v18, 2, v0
	s_movk_i32 s4, 0x3c0
	v_or3_b32 v2, v2, v3, v4
	v_and_or_b32 v10, v18, s4, v3
	ds_write_b32 v2, a4
	ds_write_b32 v2, a0 offset:1024
	ds_write_b32 v2, a5 offset:64
	ds_write_b32 v2, a1 offset:1088
	ds_write_b32 v2, a6 offset:128
	ds_write_b32 v2, a2 offset:1152
	ds_write_b32 v2, a7 offset:192
	ds_write_b32 v2, a3 offset:1216
	s_waitcnt lgkmcnt(0)
	s_barrier
	ds_read2st64_b32 v[2:3], v10 offset1:4
	ds_read2st64_b32 v[4:5], v10 offset0:8 offset1:12
	ds_read2st64_b32 v[6:7], v10 offset0:16 offset1:20
	ds_read2st64_b32 v[8:9], v10 offset0:24 offset1:28
	s_movk_i32 s4, 0x1000
	v_or_b32_e32 v20, 0x2000, v18
	s_waitcnt lgkmcnt(2)
	v_add_f32_e32 v2, v2, v4
	v_add_f32_e32 v3, v3, v5
	s_waitcnt lgkmcnt(1)
	v_add_f32_e32 v2, v2, v6
	v_add_f32_e32 v3, v3, v7
	v_lshl_add_u64 v[6:7], s[6:7], 0, v[18:19]
	s_waitcnt lgkmcnt(0)
	v_add_f32_e32 v2, v2, v8
	v_add_f32_e32 v3, v3, v9
	v_add_co_u32_e32 v4, vcc, s4, v6
	ds_write2st64_b32 v10, v2, v3 offset0:32 offset1:36
	v_or_b32_e32 v10, 0x1000, v18
	v_addc_co_u32_e32 v5, vcc, 0, v7, vcc
	s_waitcnt lgkmcnt(0)
	s_barrier
	global_load_dword v2, v18, s[6:7] offset:2048
	global_load_dword v3, v18, s[6:7] offset:3072
	global_load_dword v57, v10, s[6:7]
	global_load_dword v49, v[4:5], off offset:1024
	global_load_dword v50, v[4:5], off offset:2048
	global_load_dword v44, v[4:5], off offset:3072
	global_load_dword v51, v10, s[16:17]
	global_load_dword v13, v18, s[6:7]
	s_nop 0
	global_load_dword v5, v18, s[16:17]
	global_load_dword v10, v18, s[6:7] offset:1024
	global_load_dword v11, v18, s[16:17] offset:1024
	global_load_dword v4, v18, s[16:17] offset:2048
	global_load_dword v42, v18, s[8:9]
	global_load_dword v12, v18, s[16:17] offset:3072
	global_load_dword v40, v18, s[18:19]
	v_lshl_add_u64 v[8:9], s[16:17], 0, v[18:19]
	v_add_co_u32_e32 v14, vcc, s4, v8
	s_movk_i32 s4, 0x2000
	s_nop 0
	v_addc_co_u32_e32 v15, vcc, 0, v9, vcc
	v_add_co_u32_e32 v16, vcc, s4, v6
	s_mov_b32 s5, 0xc2000000
	s_nop 0
	v_addc_co_u32_e32 v17, vcc, 0, v7, vcc
	global_load_dword v56, v[14:15], off offset:1024
	global_load_dword v54, v[14:15], off offset:2048
	global_load_dword v52, v[14:15], off offset:3072
	global_load_dword v53, v20, s[6:7]
	global_load_dword v43, v[16:17], off offset:1024
	global_load_dword v30, v[16:17], off offset:2048
	global_load_dword v31, v[16:17], off offset:3072
	global_load_dword v45, v20, s[16:17]
	v_add_co_u32_e32 v14, vcc, s4, v8
	s_movk_i32 s4, 0x3000
	s_nop 0
	v_addc_co_u32_e32 v15, vcc, 0, v9, vcc
	v_add_co_u32_e32 v6, vcc, s4, v6
	v_or_b32_e32 v16, 0x3000, v18
	s_nop 0
	v_addc_co_u32_e32 v7, vcc, 0, v7, vcc
	global_load_dword v46, v[14:15], off offset:1024
	global_load_dword v34, v[14:15], off offset:2048
	global_load_dword v35, v[14:15], off offset:3072
	global_load_dword v32, v16, s[6:7]
	global_load_dword v33, v[6:7], off offset:1024
	global_load_dword v20, v[6:7], off offset:2048
	global_load_dword v21, v[6:7], off offset:3072
	global_load_dword v22, v16, s[16:17]
	v_add_co_u32_e32 v6, vcc, s4, v8
	s_and_b32 s4, s2, 0xffffff80
	s_nop 0
	v_addc_co_u32_e32 v7, vcc, 0, v9, vcc
	global_load_dword v23, v[6:7], off offset:1024
	global_load_dword v24, v[6:7], off offset:2048
	global_load_dword v25, v[6:7], off offset:3072
	v_lshl_or_b32 v6, v1, 5, s4
	s_lshr_b32 s4, s2, 2
	v_and_or_b32 v70, s4, 31, v6
	ds_read_b128 v[6:9], v19 offset:8192
	ds_read_b128 v[14:17], v19 offset:9216
	ds_read_b128 v[26:29], v19 offset:8208
	ds_read_b128 v[58:61], v19 offset:8224
	ds_read_b128 v[62:65], v19 offset:8240
	v_lshlrev_b32_e32 v18, 1, v36
	ds_read_b128 v[66:69], v19 offset:9232
	v_lshl_add_u64 v[72:73], s[24:25], 0, v[18:19]
	v_mov_b32_e32 v38, 0x42000000
	v_ashrrev_i32_e32 v71, 31, v70
	s_and_b32 s4, s22, 48
	s_lshl_b32 s22, s4, 7
	s_lshl_b32 s4, s4, 1
	s_waitcnt vmcnt(21) lgkmcnt(5)
	v_fma_f32 v18, v13, v6, v42
	v_fmac_f32_e32 v18, v10, v7
	s_waitcnt vmcnt(19) lgkmcnt(4)
	v_fma_f32 v37, v5, v14, v40
	v_fmac_f32_e32 v37, v11, v15
	v_fmac_f32_e32 v18, v2, v8
	v_fmac_f32_e32 v37, v4, v16
	v_fmac_f32_e32 v18, v3, v9
	v_fmac_f32_e32 v37, v12, v17
	ds_read_b128 v[6:9], v19 offset:9248
	s_waitcnt lgkmcnt(4)
	v_fmac_f32_e32 v18, v57, v26
	s_waitcnt lgkmcnt(1)
	v_fmac_f32_e32 v37, v51, v66
	v_fmac_f32_e32 v18, v49, v27
	s_waitcnt vmcnt(18)
	v_fmac_f32_e32 v37, v56, v67
	v_fmac_f32_e32 v18, v50, v28
	s_waitcnt vmcnt(17)
	v_fmac_f32_e32 v37, v54, v68
	v_fmac_f32_e32 v18, v44, v29
	s_waitcnt vmcnt(16)
	v_fmac_f32_e32 v37, v52, v69
	s_waitcnt vmcnt(15)
	v_fmac_f32_e32 v18, v53, v58
	s_waitcnt vmcnt(11) lgkmcnt(0)
	v_fmac_f32_e32 v37, v45, v6
	v_fmac_f32_e32 v18, v43, v59
	s_waitcnt vmcnt(10)
	v_fmac_f32_e32 v37, v46, v7
	v_pk_mul_f32 v[6:7], v[30:31], v[60:61]
	ds_read_b128 v[14:17], v19 offset:9264
	v_add_f32_e32 v6, v18, v6
	v_add_f32_e32 v18, v6, v7
	s_waitcnt vmcnt(8)
	v_pk_mul_f32 v[6:7], v[34:35], v[8:9]
	v_lshlrev_b64 v[26:27], 13, v[70:71]
	v_add_f32_e32 v6, v37, v6
	v_add_f32_e32 v8, v6, v7
	s_waitcnt vmcnt(6)
	v_pk_mul_f32 v[6:7], v[32:33], v[62:63]
	s_nop 0
	v_add_f32_e32 v6, v18, v6
	v_add_f32_e32 v9, v6, v7
	s_waitcnt vmcnt(2) lgkmcnt(0)
	v_pk_mul_f32 v[6:7], v[22:23], v[14:15]
	s_nop 0
	v_add_f32_e32 v6, v8, v6
	v_add_f32_e32 v8, v6, v7
	v_pk_mul_f32 v[6:7], v[20:21], v[64:65]
	s_nop 0
	v_add_f32_e32 v6, v9, v6
	v_add_f32_e32 v9, v6, v7
	s_waitcnt vmcnt(0)
	v_pk_mul_f32 v[6:7], v[24:25], v[16:17]
	s_nop 0
	v_add_f32_e32 v6, v8, v6
	v_add_f32_e32 v6, v6, v7
	v_med3_f32 v6, v6, s5, v38
	v_mul_f32_e32 v6, 0x3fb8aa3b, v6
	v_exp_f32_e32 v18, v6
	v_med3_f32 v6, v9, s5, v38
	v_mul_f32_e32 v6, 0x3fb8aa3b, v6
	v_exp_f32_e32 v37, v6
	v_lshl_add_u64 v[6:7], v[72:73], 0, v[26:27]
	v_cvt_pk_bf16_f32 v8, v18, s0
	v_lshl_add_u64 v[28:29], v[6:7], 0, s[22:23]
	global_store_short v[28:29], v8, off
	ds_read_b128 v[6:9], v19 offset:8256
	ds_read_b128 v[14:17], v19 offset:9280
	ds_read_b128 v[58:61], v19 offset:8272
	ds_read_b128 v[62:65], v19 offset:8288
	ds_read_b128 v[66:69], v19 offset:8304
	ds_read_b128 v[70:73], v19 offset:9296
	s_waitcnt lgkmcnt(5)
	v_fma_f32 v39, v13, v6, v42
	s_waitcnt lgkmcnt(4)
	v_fma_f32 v41, v5, v14, v40
	v_fmac_f32_e32 v39, v10, v7
	v_fmac_f32_e32 v41, v11, v15
	v_fmac_f32_e32 v39, v2, v8
	v_fmac_f32_e32 v41, v4, v16
	v_fmac_f32_e32 v39, v3, v9
	v_fmac_f32_e32 v41, v12, v17
	ds_read_b128 v[6:9], v19 offset:9312
	s_waitcnt lgkmcnt(4)
	v_fmac_f32_e32 v39, v57, v58
	s_waitcnt lgkmcnt(1)
	v_fmac_f32_e32 v41, v51, v70
	v_fmac_f32_e32 v39, v49, v59
	v_fmac_f32_e32 v41, v56, v71
	v_fmac_f32_e32 v39, v50, v60
	v_fmac_f32_e32 v41, v54, v72
	v_fmac_f32_e32 v39, v44, v61
	v_fmac_f32_e32 v41, v52, v73
	v_fmac_f32_e32 v39, v53, v62
	s_waitcnt lgkmcnt(0)
	v_fmac_f32_e32 v41, v45, v6
	v_fmac_f32_e32 v39, v43, v63
	v_fmac_f32_e32 v41, v46, v7
	v_pk_mul_f32 v[6:7], v[30:31], v[64:65]
	ds_read_b128 v[14:17], v19 offset:9328
	v_add_f32_e32 v6, v39, v6
	v_add_f32_e32 v39, v6, v7
	v_pk_mul_f32 v[6:7], v[34:35], v[8:9]
	s_nop 0
	v_add_f32_e32 v6, v41, v6
	v_add_f32_e32 v8, v6, v7
	v_pk_mul_f32 v[6:7], v[32:33], v[66:67]
	s_nop 0
	v_add_f32_e32 v6, v39, v6
	v_add_f32_e32 v9, v6, v7
	s_waitcnt lgkmcnt(0)
	v_pk_mul_f32 v[6:7], v[22:23], v[14:15]
	s_nop 0
	v_add_f32_e32 v6, v8, v6
	v_add_f32_e32 v8, v6, v7
	v_pk_mul_f32 v[6:7], v[20:21], v[68:69]
	s_nop 0
	v_add_f32_e32 v6, v9, v6
	v_add_f32_e32 v9, v6, v7
	v_pk_mul_f32 v[6:7], v[24:25], v[16:17]
	s_nop 0
	v_add_f32_e32 v6, v8, v6
	v_add_f32_e32 v6, v6, v7
	v_med3_f32 v6, v6, s5, v38
	v_mul_f32_e32 v6, 0x3fb8aa3b, v6
	v_med3_f32 v7, v9, s5, v38
	v_exp_f32_e32 v39, v6
	v_mul_f32_e32 v41, 0x3fb8aa3b, v7
	ds_read_b128 v[6:9], v19 offset:8320
	ds_read_b128 v[14:17], v19 offset:9344
	ds_read_b128 v[58:61], v19 offset:8336
	ds_read_b128 v[62:65], v19 offset:9360
	v_cvt_pk_bf16_f32 v47, v39, s0
	global_store_short v[28:29], v47, off offset:128
	s_waitcnt lgkmcnt(3)
	v_fma_f32 v47, v13, v6, v42
	s_waitcnt lgkmcnt(2)
	v_fma_f32 v48, v5, v14, v40
	v_fmac_f32_e32 v47, v10, v7
	v_fmac_f32_e32 v48, v11, v15
	v_fmac_f32_e32 v47, v2, v8
	v_fmac_f32_e32 v48, v4, v16
	v_fmac_f32_e32 v47, v3, v9
	v_fmac_f32_e32 v48, v12, v17
	s_waitcnt lgkmcnt(1)
	v_fmac_f32_e32 v47, v57, v58
	ds_read_b128 v[6:9], v19 offset:8352
	ds_read_b128 v[14:17], v19 offset:9376
	v_fmac_f32_e32 v47, v49, v59
	s_waitcnt lgkmcnt(2)
	v_fmac_f32_e32 v48, v51, v62
	v_fmac_f32_e32 v47, v50, v60
	v_fmac_f32_e32 v48, v56, v63
	v_fmac_f32_e32 v47, v44, v61
	v_fmac_f32_e32 v48, v54, v64
	ds_read_b128 v[58:61], v19 offset:8368
	s_waitcnt lgkmcnt(2)
	v_fmac_f32_e32 v47, v53, v6
	v_fmac_f32_e32 v48, v52, v65
	v_fmac_f32_e32 v47, v43, v7
	v_pk_mul_f32 v[6:7], v[30:31], v[8:9]
	ds_read_b128 v[62:65], v19 offset:9392
	s_waitcnt lgkmcnt(2)
	v_fmac_f32_e32 v48, v45, v14
	v_add_f32_e32 v6, v47, v6
	v_fmac_f32_e32 v48, v46, v15
	v_add_f32_e32 v8, v6, v7
	v_pk_mul_f32 v[6:7], v[34:35], v[16:17]
	v_exp_f32_e32 v41, v41
	v_add_f32_e32 v6, v48, v6
	v_add_f32_e32 v9, v6, v7
	s_waitcnt lgkmcnt(1)
	v_pk_mul_f32 v[6:7], v[32:33], v[58:59]
	s_nop 0
	v_add_f32_e32 v6, v8, v6
	v_add_f32_e32 v8, v6, v7
	s_waitcnt lgkmcnt(0)
	v_pk_mul_f32 v[6:7], v[22:23], v[62:63]
	s_nop 0
	v_add_f32_e32 v6, v9, v6
	v_add_f32_e32 v9, v6, v7
	v_pk_mul_f32 v[6:7], v[20:21], v[60:61]
	s_nop 0
	v_add_f32_e32 v6, v8, v6
	v_add_f32_e32 v8, v6, v7
	v_pk_mul_f32 v[6:7], v[24:25], v[64:65]
	s_nop 0
	v_add_f32_e32 v6, v9, v6
	v_add_f32_e32 v6, v6, v7
	v_med3_f32 v6, v6, s5, v38
	v_mul_f32_e32 v6, 0x3fb8aa3b, v6
	v_exp_f32_e32 v47, v6
	v_med3_f32 v6, v8, s5, v38
	v_mul_f32_e32 v6, 0x3fb8aa3b, v6
	v_exp_f32_e32 v48, v6
	v_cvt_pk_bf16_f32 v6, v47, s0
	global_store_short v[28:29], v6, off offset:256
	ds_read_b128 v[6:9], v19 offset:8384
	ds_read_b128 v[14:17], v19 offset:9408
	ds_read_b128 v[58:61], v19 offset:8400
	ds_read_b128 v[62:65], v19 offset:8416
	ds_read_b128 v[66:69], v19 offset:8432
	ds_read_b128 v[70:73], v19 offset:9424
	s_waitcnt lgkmcnt(5)
	v_fma_f32 v55, v13, v6, v42
	s_waitcnt lgkmcnt(4)
	v_fma_f32 v74, v5, v14, v40
	v_fmac_f32_e32 v55, v10, v7
	v_fmac_f32_e32 v74, v11, v15
	v_fmac_f32_e32 v55, v2, v8
	v_fmac_f32_e32 v74, v4, v16
	v_fmac_f32_e32 v55, v3, v9
	v_fmac_f32_e32 v74, v12, v17
	ds_read_b128 v[6:9], v19 offset:9440
	s_waitcnt lgkmcnt(4)
	v_fmac_f32_e32 v55, v57, v58
	s_waitcnt lgkmcnt(1)
	v_fmac_f32_e32 v74, v51, v70
	v_fmac_f32_e32 v55, v49, v59
	v_fmac_f32_e32 v74, v56, v71
	v_fmac_f32_e32 v55, v50, v60
	v_fmac_f32_e32 v74, v54, v72
	v_fmac_f32_e32 v55, v44, v61
	v_fmac_f32_e32 v74, v52, v73
	v_fmac_f32_e32 v55, v53, v62
	s_waitcnt lgkmcnt(0)
	v_fmac_f32_e32 v74, v45, v6
	v_fmac_f32_e32 v55, v43, v63
	v_fmac_f32_e32 v74, v46, v7
	v_pk_mul_f32 v[6:7], v[30:31], v[64:65]
	ds_read_b128 v[14:17], v19 offset:9456
	v_add_f32_e32 v6, v55, v6
	v_add_f32_e32 v55, v6, v7
	v_pk_mul_f32 v[6:7], v[34:35], v[8:9]
	s_nop 0
	v_add_f32_e32 v6, v74, v6
	v_add_f32_e32 v8, v6, v7
	v_pk_mul_f32 v[6:7], v[32:33], v[66:67]
	s_nop 0
	v_add_f32_e32 v6, v55, v6
	v_add_f32_e32 v9, v6, v7
	s_waitcnt lgkmcnt(0)
	v_pk_mul_f32 v[6:7], v[22:23], v[14:15]
	s_nop 0
	v_add_f32_e32 v6, v8, v6
	v_add_f32_e32 v8, v6, v7
	v_pk_mul_f32 v[6:7], v[20:21], v[68:69]
	s_nop 0
	v_add_f32_e32 v6, v9, v6
	v_add_f32_e32 v9, v6, v7
	v_pk_mul_f32 v[6:7], v[24:25], v[16:17]
	s_nop 0
	v_add_f32_e32 v6, v8, v6
	v_add_f32_e32 v6, v6, v7
	v_med3_f32 v6, v6, s5, v38
	v_mul_f32_e32 v6, 0x3fb8aa3b, v6
	v_med3_f32 v7, v9, s5, v38
	v_exp_f32_e32 v55, v6
	v_mul_f32_e32 v58, 0x3fb8aa3b, v7
	ds_read_b128 v[6:9], v19 offset:8448
	ds_read_b128 v[14:17], v19 offset:9472
	ds_read_b128 v[60:63], v19 offset:8464
	ds_read_b128 v[64:67], v19 offset:9488
	v_cvt_pk_bf16_f32 v59, v55, s0
	global_store_short v[28:29], v59, off offset:384
	s_waitcnt lgkmcnt(3)
	v_fma_f32 v59, v13, v6, v42
	s_waitcnt lgkmcnt(2)
	v_fma_f32 v68, v5, v14, v40
	v_fmac_f32_e32 v59, v10, v7
	v_fmac_f32_e32 v68, v11, v15
	v_fmac_f32_e32 v59, v2, v8
	v_fmac_f32_e32 v68, v4, v16
	v_fmac_f32_e32 v59, v3, v9
	v_fmac_f32_e32 v68, v12, v17
	s_waitcnt lgkmcnt(1)
	v_fmac_f32_e32 v59, v57, v60
	ds_read_b128 v[6:9], v19 offset:8480
	ds_read_b128 v[14:17], v19 offset:9504
	v_fmac_f32_e32 v59, v49, v61
	s_waitcnt lgkmcnt(2)
	v_fmac_f32_e32 v68, v51, v64
	v_fmac_f32_e32 v59, v50, v62
	v_fmac_f32_e32 v68, v56, v65
	v_fmac_f32_e32 v59, v44, v63
	v_fmac_f32_e32 v68, v54, v66
	ds_read_b128 v[60:63], v19 offset:8496
	s_waitcnt lgkmcnt(2)
	v_fmac_f32_e32 v59, v53, v6
	v_fmac_f32_e32 v68, v52, v67
	v_fmac_f32_e32 v59, v43, v7
	v_pk_mul_f32 v[6:7], v[30:31], v[8:9]
	ds_read_b128 v[64:67], v19 offset:9520
	s_waitcnt lgkmcnt(2)
	v_fmac_f32_e32 v68, v45, v14
	v_add_f32_e32 v6, v59, v6
	v_fmac_f32_e32 v68, v46, v15
	v_add_f32_e32 v8, v6, v7
	v_pk_mul_f32 v[6:7], v[34:35], v[16:17]
	v_exp_f32_e32 v58, v58
	v_add_f32_e32 v6, v68, v6
	v_add_f32_e32 v9, v6, v7
	s_waitcnt lgkmcnt(1)
	v_pk_mul_f32 v[6:7], v[32:33], v[60:61]
	s_nop 0
	v_add_f32_e32 v6, v8, v6
	v_add_f32_e32 v8, v6, v7
	s_waitcnt lgkmcnt(0)
	v_pk_mul_f32 v[6:7], v[22:23], v[64:65]
	s_nop 0
	v_add_f32_e32 v6, v9, v6
	v_add_f32_e32 v9, v6, v7
	v_pk_mul_f32 v[6:7], v[20:21], v[62:63]
	s_nop 0
	v_add_f32_e32 v6, v8, v6
	v_add_f32_e32 v8, v6, v7
	v_pk_mul_f32 v[6:7], v[24:25], v[66:67]
	s_nop 0
	v_add_f32_e32 v6, v9, v6
	v_add_f32_e32 v6, v6, v7
	v_med3_f32 v6, v6, s5, v38
	v_mul_f32_e32 v6, 0x3fb8aa3b, v6
	v_exp_f32_e32 v59, v6
	v_med3_f32 v6, v8, s5, v38
	v_mul_f32_e32 v6, 0x3fb8aa3b, v6
	v_exp_f32_e32 v60, v6
	v_cvt_pk_bf16_f32 v6, v59, s0
	global_store_short v[28:29], v6, off offset:512
	ds_read_b128 v[6:9], v19 offset:8512
	ds_read_b128 v[14:17], v19 offset:9536
	ds_read_b128 v[62:65], v19 offset:8528
	ds_read_b128 v[66:69], v19 offset:8544
	ds_read_b128 v[70:73], v19 offset:8560
	ds_read_b128 v[74:77], v19 offset:9552
	s_waitcnt lgkmcnt(5)
	v_fma_f32 v61, v13, v6, v42
	s_waitcnt lgkmcnt(4)
	v_fma_f32 v78, v5, v14, v40
	v_fmac_f32_e32 v61, v10, v7
	v_fmac_f32_e32 v78, v11, v15
	v_fmac_f32_e32 v61, v2, v8
	v_fmac_f32_e32 v78, v4, v16
	v_fmac_f32_e32 v61, v3, v9
	v_fmac_f32_e32 v78, v12, v17
	ds_read_b128 v[6:9], v19 offset:9568
	s_waitcnt lgkmcnt(4)
	v_fmac_f32_e32 v61, v57, v62
	s_waitcnt lgkmcnt(1)
	v_fmac_f32_e32 v78, v51, v74
	v_fmac_f32_e32 v61, v49, v63
	v_fmac_f32_e32 v78, v56, v75
	v_fmac_f32_e32 v61, v50, v64
	v_fmac_f32_e32 v78, v54, v76
	v_fmac_f32_e32 v61, v44, v65
	v_fmac_f32_e32 v78, v52, v77
	v_fmac_f32_e32 v61, v53, v66
	s_waitcnt lgkmcnt(0)
	v_fmac_f32_e32 v78, v45, v6
	v_fmac_f32_e32 v61, v43, v67
	v_fmac_f32_e32 v78, v46, v7
	v_pk_mul_f32 v[6:7], v[30:31], v[68:69]
	ds_read_b128 v[14:17], v19 offset:9584
	v_add_f32_e32 v6, v61, v6
	v_add_f32_e32 v61, v6, v7
	v_pk_mul_f32 v[6:7], v[34:35], v[8:9]
	s_nop 0
	v_add_f32_e32 v6, v78, v6
	v_add_f32_e32 v8, v6, v7
	v_pk_mul_f32 v[6:7], v[32:33], v[70:71]
	s_nop 0
	v_add_f32_e32 v6, v61, v6
	v_add_f32_e32 v9, v6, v7
	s_waitcnt lgkmcnt(0)
	v_pk_mul_f32 v[6:7], v[22:23], v[14:15]
	s_nop 0
	v_add_f32_e32 v6, v8, v6
	v_add_f32_e32 v8, v6, v7
	v_pk_mul_f32 v[6:7], v[20:21], v[72:73]
	s_nop 0
	v_add_f32_e32 v6, v9, v6
	v_add_f32_e32 v9, v6, v7
	v_pk_mul_f32 v[6:7], v[24:25], v[16:17]
	s_nop 0
	v_add_f32_e32 v6, v8, v6
	v_add_f32_e32 v6, v6, v7
	v_med3_f32 v6, v6, s5, v38
	v_mul_f32_e32 v6, 0x3fb8aa3b, v6
	v_med3_f32 v7, v9, s5, v38
	v_exp_f32_e32 v61, v6
	v_mul_f32_e32 v62, 0x3fb8aa3b, v7
	ds_read_b128 v[6:9], v19 offset:8576
	ds_read_b128 v[14:17], v19 offset:9600
	ds_read_b128 v[64:67], v19 offset:8592
	ds_read_b128 v[68:71], v19 offset:9616
	v_cvt_pk_bf16_f32 v63, v61, s0
	global_store_short v[28:29], v63, off offset:640
	s_waitcnt lgkmcnt(3)
	v_fma_f32 v63, v13, v6, v42
	s_waitcnt lgkmcnt(2)
	v_fma_f32 v72, v5, v14, v40
	v_fmac_f32_e32 v63, v10, v7
	v_fmac_f32_e32 v72, v11, v15
	v_fmac_f32_e32 v63, v2, v8
	v_fmac_f32_e32 v72, v4, v16
	v_fmac_f32_e32 v63, v3, v9
	v_fmac_f32_e32 v72, v12, v17
	s_waitcnt lgkmcnt(1)
	v_fmac_f32_e32 v63, v57, v64
	ds_read_b128 v[6:9], v19 offset:8608
	ds_read_b128 v[14:17], v19 offset:9632
	v_fmac_f32_e32 v63, v49, v65
	s_waitcnt lgkmcnt(2)
	v_fmac_f32_e32 v72, v51, v68
	v_fmac_f32_e32 v63, v50, v66
	v_fmac_f32_e32 v72, v56, v69
	v_fmac_f32_e32 v63, v44, v67
	v_fmac_f32_e32 v72, v54, v70
	ds_read_b128 v[64:67], v19 offset:8624
	s_waitcnt lgkmcnt(2)
	v_fmac_f32_e32 v63, v53, v6
	v_fmac_f32_e32 v72, v52, v71
	v_fmac_f32_e32 v63, v43, v7
	v_pk_mul_f32 v[6:7], v[30:31], v[8:9]
	ds_read_b128 v[68:71], v19 offset:9648
	s_waitcnt lgkmcnt(2)
	v_fmac_f32_e32 v72, v45, v14
	v_add_f32_e32 v6, v63, v6
	v_fmac_f32_e32 v72, v46, v15
	v_add_f32_e32 v8, v6, v7
	v_pk_mul_f32 v[6:7], v[34:35], v[16:17]
	v_exp_f32_e32 v62, v62
	v_add_f32_e32 v6, v72, v6
	v_add_f32_e32 v9, v6, v7
	s_waitcnt lgkmcnt(1)
	v_pk_mul_f32 v[6:7], v[32:33], v[64:65]
	s_nop 0
	v_add_f32_e32 v6, v8, v6
	v_add_f32_e32 v8, v6, v7
	s_waitcnt lgkmcnt(0)
	v_pk_mul_f32 v[6:7], v[22:23], v[68:69]
	s_nop 0
	v_add_f32_e32 v6, v9, v6
	v_add_f32_e32 v9, v6, v7
	v_pk_mul_f32 v[6:7], v[20:21], v[66:67]
	s_nop 0
	v_add_f32_e32 v6, v8, v6
	v_add_f32_e32 v8, v6, v7
	v_pk_mul_f32 v[6:7], v[24:25], v[70:71]
	s_nop 0
	v_add_f32_e32 v6, v9, v6
	v_add_f32_e32 v6, v6, v7
	v_med3_f32 v6, v6, s5, v38
	v_mul_f32_e32 v6, 0x3fb8aa3b, v6
	v_exp_f32_e32 v63, v6
	v_med3_f32 v6, v8, s5, v38
	v_mul_f32_e32 v6, 0x3fb8aa3b, v6
	v_exp_f32_e32 v64, v6
	v_cvt_pk_bf16_f32 v6, v63, s0
	global_store_short v[28:29], v6, off offset:768
	ds_read_b128 v[6:9], v19 offset:8640
	ds_read_b128 v[14:17], v19 offset:9664
	ds_read_b128 v[66:69], v19 offset:8656
	ds_read_b128 v[70:73], v19 offset:8672
	ds_read_b128 v[74:77], v19 offset:8688
	ds_read_b128 v[78:81], v19 offset:9680
	s_waitcnt lgkmcnt(5)
	v_fma_f32 v65, v13, v6, v42
	s_waitcnt lgkmcnt(4)
	v_fma_f32 v82, v5, v14, v40
	v_fmac_f32_e32 v65, v10, v7
	v_fmac_f32_e32 v82, v11, v15
	v_fmac_f32_e32 v65, v2, v8
	v_fmac_f32_e32 v82, v4, v16
	v_fmac_f32_e32 v65, v3, v9
	v_fmac_f32_e32 v82, v12, v17
	ds_read_b128 v[6:9], v19 offset:9696
	s_waitcnt lgkmcnt(4)
	v_fmac_f32_e32 v65, v57, v66
	s_waitcnt lgkmcnt(1)
	v_fmac_f32_e32 v82, v51, v78
	v_fmac_f32_e32 v65, v49, v67
	v_fmac_f32_e32 v82, v56, v79
	v_fmac_f32_e32 v65, v50, v68
	v_fmac_f32_e32 v82, v54, v80
	v_fmac_f32_e32 v65, v44, v69
	v_fmac_f32_e32 v82, v52, v81
	v_fmac_f32_e32 v65, v53, v70
	s_waitcnt lgkmcnt(0)
	v_fmac_f32_e32 v82, v45, v6
	v_fmac_f32_e32 v65, v43, v71
	v_fmac_f32_e32 v82, v46, v7
	v_pk_mul_f32 v[6:7], v[30:31], v[72:73]
	ds_read_b128 v[14:17], v19 offset:9712
	v_add_f32_e32 v6, v65, v6
	v_add_f32_e32 v65, v6, v7
	v_pk_mul_f32 v[6:7], v[34:35], v[8:9]
	s_nop 0
	v_add_f32_e32 v6, v82, v6
	v_add_f32_e32 v8, v6, v7
	v_pk_mul_f32 v[6:7], v[32:33], v[74:75]
	s_nop 0
	v_add_f32_e32 v6, v65, v6
	v_add_f32_e32 v9, v6, v7
	s_waitcnt lgkmcnt(0)
	v_pk_mul_f32 v[6:7], v[22:23], v[14:15]
	s_nop 0
	v_add_f32_e32 v6, v8, v6
	v_add_f32_e32 v8, v6, v7
	v_pk_mul_f32 v[6:7], v[20:21], v[76:77]
	s_nop 0
	v_add_f32_e32 v6, v9, v6
	v_add_f32_e32 v9, v6, v7
	v_pk_mul_f32 v[6:7], v[24:25], v[16:17]
	s_nop 0
	v_add_f32_e32 v6, v8, v6
	v_add_f32_e32 v6, v6, v7
	v_med3_f32 v6, v6, s5, v38
	v_mul_f32_e32 v6, 0x3fb8aa3b, v6
	v_exp_f32_e32 v65, v6
	v_med3_f32 v6, v9, s5, v38
	v_mul_f32_e32 v6, 0x3fb8aa3b, v6
	v_exp_f32_e32 v66, v6
	v_cvt_pk_bf16_f32 v6, v65, s0
	global_store_short v[28:29], v6, off offset:896
	ds_read_b128 v[6:9], v19 offset:8704
	ds_read_b128 v[14:17], v19 offset:9728
	ds_read_b128 v[68:71], v19 offset:8720
	ds_read_b128 v[72:75], v19 offset:8736
	ds_read_b128 v[76:79], v19 offset:8752
	ds_read_b128 v[80:83], v19 offset:9744
	s_waitcnt lgkmcnt(5)
	v_fma_f32 v67, v13, v6, v42
	s_waitcnt lgkmcnt(4)
	v_fma_f32 v84, v5, v14, v40
	v_fmac_f32_e32 v67, v10, v7
	v_fmac_f32_e32 v84, v11, v15
	v_fmac_f32_e32 v67, v2, v8
	v_fmac_f32_e32 v84, v4, v16
	v_fmac_f32_e32 v67, v3, v9
	v_fmac_f32_e32 v84, v12, v17
	ds_read_b128 v[6:9], v19 offset:9760
	s_waitcnt lgkmcnt(4)
	v_fmac_f32_e32 v67, v57, v68
	s_waitcnt lgkmcnt(1)
	v_fmac_f32_e32 v84, v51, v80
	v_fmac_f32_e32 v67, v49, v69
	v_fmac_f32_e32 v84, v56, v81
	v_fmac_f32_e32 v67, v50, v70
	v_fmac_f32_e32 v84, v54, v82
	v_fmac_f32_e32 v67, v44, v71
	v_fmac_f32_e32 v84, v52, v83
	v_fmac_f32_e32 v67, v53, v72
	s_waitcnt lgkmcnt(0)
	v_fmac_f32_e32 v84, v45, v6
	v_fmac_f32_e32 v67, v43, v73
	v_fmac_f32_e32 v84, v46, v7
	v_pk_mul_f32 v[6:7], v[30:31], v[74:75]
	ds_read_b128 v[14:17], v19 offset:9776
	v_add_f32_e32 v6, v67, v6
	v_add_f32_e32 v67, v6, v7
	v_pk_mul_f32 v[6:7], v[34:35], v[8:9]
	s_nop 0
	v_add_f32_e32 v6, v84, v6
	v_add_f32_e32 v8, v6, v7
	v_pk_mul_f32 v[6:7], v[32:33], v[76:77]
	s_nop 0
	v_add_f32_e32 v6, v67, v6
	v_add_f32_e32 v9, v6, v7
	s_waitcnt lgkmcnt(0)
	v_pk_mul_f32 v[6:7], v[22:23], v[14:15]
	s_nop 0
	v_add_f32_e32 v6, v8, v6
	v_add_f32_e32 v8, v6, v7
	v_pk_mul_f32 v[6:7], v[20:21], v[78:79]
	s_nop 0
	v_add_f32_e32 v6, v9, v6
	v_add_f32_e32 v9, v6, v7
	v_pk_mul_f32 v[6:7], v[24:25], v[16:17]
	s_nop 0
	v_add_f32_e32 v6, v8, v6
	v_add_f32_e32 v6, v6, v7
	v_med3_f32 v6, v6, s5, v38
	v_mul_f32_e32 v6, 0x3fb8aa3b, v6
	v_exp_f32_e32 v67, v6
	v_med3_f32 v6, v9, s5, v38
	v_mul_f32_e32 v6, 0x3fb8aa3b, v6
	v_exp_f32_e32 v68, v6
	v_cvt_pk_bf16_f32 v6, v67, s0
	global_store_short v[28:29], v6, off offset:1024
	ds_read_b128 v[6:9], v19 offset:8768
	ds_read_b128 v[14:17], v19 offset:9792
	ds_read_b128 v[70:73], v19 offset:8784
	ds_read_b128 v[74:77], v19 offset:8800
	ds_read_b128 v[78:81], v19 offset:8816
	ds_read_b128 v[82:85], v19 offset:9808
	s_waitcnt lgkmcnt(5)
	v_fma_f32 v69, v13, v6, v42
	s_waitcnt lgkmcnt(4)
	v_fma_f32 v86, v5, v14, v40
	v_fmac_f32_e32 v69, v10, v7
	v_fmac_f32_e32 v86, v11, v15
	v_fmac_f32_e32 v69, v2, v8
	v_fmac_f32_e32 v86, v4, v16
	v_fmac_f32_e32 v69, v3, v9
	v_fmac_f32_e32 v86, v12, v17
	ds_read_b128 v[6:9], v19 offset:9824
	s_waitcnt lgkmcnt(4)
	v_fmac_f32_e32 v69, v57, v70
	s_waitcnt lgkmcnt(1)
	v_fmac_f32_e32 v86, v51, v82
	v_fmac_f32_e32 v69, v49, v71
	v_fmac_f32_e32 v86, v56, v83
	v_fmac_f32_e32 v69, v50, v72
	v_fmac_f32_e32 v86, v54, v84
	v_fmac_f32_e32 v69, v44, v73
	v_fmac_f32_e32 v86, v52, v85
	v_fmac_f32_e32 v69, v53, v74
	s_waitcnt lgkmcnt(0)
	v_fmac_f32_e32 v86, v45, v6
	v_fmac_f32_e32 v69, v43, v75
	v_fmac_f32_e32 v86, v46, v7
	v_pk_mul_f32 v[6:7], v[30:31], v[76:77]
	ds_read_b128 v[14:17], v19 offset:9840
	v_add_f32_e32 v6, v69, v6
	v_add_f32_e32 v69, v6, v7
	v_pk_mul_f32 v[6:7], v[34:35], v[8:9]
	ds_read_b128 v[72:75], v19 offset:8848
	v_add_f32_e32 v6, v86, v6
	v_add_f32_e32 v8, v6, v7
	v_pk_mul_f32 v[6:7], v[32:33], v[78:79]
	ds_read_b128 v[76:79], v19 offset:9872
	v_add_f32_e32 v6, v69, v6
	v_add_f32_e32 v9, v6, v7
	s_waitcnt lgkmcnt(2)
	v_pk_mul_f32 v[6:7], v[22:23], v[14:15]
	s_nop 0
	v_add_f32_e32 v6, v8, v6
	v_add_f32_e32 v8, v6, v7
	v_pk_mul_f32 v[6:7], v[20:21], v[80:81]
	s_nop 0
	v_add_f32_e32 v6, v9, v6
	v_add_f32_e32 v9, v6, v7
	v_pk_mul_f32 v[6:7], v[24:25], v[16:17]
	ds_read_b128 v[14:17], v19 offset:9856
	v_add_f32_e32 v6, v8, v6
	v_add_f32_e32 v6, v6, v7
	v_med3_f32 v6, v6, s5, v38
	v_mul_f32_e32 v6, 0x3fb8aa3b, v6
	v_exp_f32_e32 v69, v6
	v_med3_f32 v6, v9, s5, v38
	v_mul_f32_e32 v6, 0x3fb8aa3b, v6
	v_exp_f32_e32 v70, v6
	ds_read_b128 v[6:9], v19 offset:8832
	v_cvt_pk_bf16_f32 v71, v69, s0
	global_store_short v[28:29], v71, off offset:1152
	s_waitcnt lgkmcnt(1)
	v_fma_f32 v80, v5, v14, v40
	v_fmac_f32_e32 v80, v11, v15
	s_waitcnt lgkmcnt(0)
	v_fma_f32 v71, v13, v6, v42
	v_fmac_f32_e32 v71, v10, v7
	v_fmac_f32_e32 v71, v2, v8
	v_fmac_f32_e32 v71, v3, v9
	v_fmac_f32_e32 v71, v57, v72
	v_fmac_f32_e32 v80, v4, v16
	v_fmac_f32_e32 v71, v49, v73
	v_fmac_f32_e32 v80, v12, v17
	ds_read_b128 v[6:9], v19 offset:8864
	ds_read_b128 v[14:17], v19 offset:8880
	v_fmac_f32_e32 v71, v50, v74
	v_fmac_f32_e32 v71, v44, v75
	ds_read_b128 v[72:75], v19 offset:9888
	v_fmac_f32_e32 v80, v51, v76
	v_fmac_f32_e32 v80, v56, v77
	v_fmac_f32_e32 v80, v54, v78
	s_waitcnt lgkmcnt(2)
	v_fmac_f32_e32 v71, v53, v6
	v_fmac_f32_e32 v80, v52, v79
	v_fmac_f32_e32 v71, v43, v7
	v_pk_mul_f32 v[6:7], v[30:31], v[8:9]
	ds_read_b128 v[76:79], v19 offset:9904
	s_waitcnt lgkmcnt(1)
	v_fmac_f32_e32 v80, v45, v72
	v_add_f32_e32 v6, v71, v6
	v_fmac_f32_e32 v80, v46, v73
	v_add_f32_e32 v8, v6, v7
	v_pk_mul_f32 v[6:7], v[34:35], v[74:75]
	s_nop 0
	v_add_f32_e32 v6, v80, v6
	v_add_f32_e32 v9, v6, v7
	v_pk_mul_f32 v[6:7], v[32:33], v[14:15]
	s_nop 0
	v_add_f32_e32 v6, v8, v6
	v_add_f32_e32 v8, v6, v7
	s_waitcnt lgkmcnt(0)
	v_pk_mul_f32 v[6:7], v[22:23], v[76:77]
	ds_read_b128 v[74:77], v19 offset:8912
	v_add_f32_e32 v6, v9, v6
	v_add_f32_e32 v9, v6, v7
	v_pk_mul_f32 v[6:7], v[20:21], v[16:17]
	ds_read_b128 v[14:17], v19 offset:9920
	v_add_f32_e32 v6, v8, v6
	v_add_f32_e32 v8, v6, v7
	v_pk_mul_f32 v[6:7], v[24:25], v[78:79]
	ds_read_b128 v[78:81], v19 offset:9936
	v_add_f32_e32 v6, v9, v6
	v_add_f32_e32 v6, v6, v7
	v_med3_f32 v6, v6, s5, v38
	v_mul_f32_e32 v6, 0x3fb8aa3b, v6
	v_exp_f32_e32 v71, v6
	v_med3_f32 v6, v8, s5, v38
	v_mul_f32_e32 v6, 0x3fb8aa3b, v6
	v_exp_f32_e32 v72, v6
	ds_read_b128 v[6:9], v19 offset:8896
	v_cvt_pk_bf16_f32 v73, v71, s0
	global_store_short v[28:29], v73, off offset:1280
	s_waitcnt lgkmcnt(2)
	v_fma_f32 v82, v5, v14, v40
	v_fmac_f32_e32 v82, v11, v15
	s_waitcnt lgkmcnt(0)
	v_fma_f32 v73, v13, v6, v42
	v_fmac_f32_e32 v73, v10, v7
	v_fmac_f32_e32 v73, v2, v8
	v_fmac_f32_e32 v73, v3, v9
	v_fmac_f32_e32 v73, v57, v74
	v_fmac_f32_e32 v82, v4, v16
	v_fmac_f32_e32 v73, v49, v75
	v_fmac_f32_e32 v82, v12, v17
	ds_read_b128 v[6:9], v19 offset:8928
	ds_read_b128 v[14:17], v19 offset:8944
	v_fmac_f32_e32 v73, v50, v76
	v_fmac_f32_e32 v73, v44, v77
	ds_read_b128 v[74:77], v19 offset:9952
	v_fmac_f32_e32 v82, v51, v78
	v_fmac_f32_e32 v82, v56, v79
	v_fmac_f32_e32 v82, v54, v80
	s_waitcnt lgkmcnt(2)
	v_fmac_f32_e32 v73, v53, v6
	v_fmac_f32_e32 v82, v52, v81
	v_fmac_f32_e32 v73, v43, v7
	v_pk_mul_f32 v[6:7], v[30:31], v[8:9]
	ds_read_b128 v[78:81], v19 offset:9968
	s_waitcnt lgkmcnt(1)
	v_fmac_f32_e32 v82, v45, v74
	v_add_f32_e32 v6, v73, v6
	v_fmac_f32_e32 v82, v46, v75
	v_add_f32_e32 v8, v6, v7
	v_pk_mul_f32 v[6:7], v[34:35], v[76:77]
	s_nop 0
	v_add_f32_e32 v6, v82, v6
	v_add_f32_e32 v9, v6, v7
	v_pk_mul_f32 v[6:7], v[32:33], v[14:15]
	s_nop 0
	v_add_f32_e32 v6, v8, v6
	v_add_f32_e32 v8, v6, v7
	s_waitcnt lgkmcnt(0)
	v_pk_mul_f32 v[6:7], v[22:23], v[78:79]
	s_nop 0
	v_add_f32_e32 v6, v9, v6
	v_add_f32_e32 v9, v6, v7
	v_pk_mul_f32 v[6:7], v[20:21], v[16:17]
	s_nop 0
	v_add_f32_e32 v6, v8, v6
	v_add_f32_e32 v8, v6, v7
	v_pk_mul_f32 v[6:7], v[24:25], v[80:81]
	s_nop 0
	v_add_f32_e32 v6, v9, v6
	v_add_f32_e32 v6, v6, v7
	v_med3_f32 v6, v6, s5, v38
	v_med3_f32 v7, v8, s5, v38
	v_mul_f32_e32 v6, 0x3fb8aa3b, v6
	v_mul_f32_e32 v7, 0x3fb8aa3b, v7
	v_exp_f32_e32 v73, v6
	v_exp_f32_e32 v74, v7
	ds_read_b128 v[6:9], v19 offset:8960
	ds_read_b128 v[14:17], v19 offset:9984
	ds_read_b128 v[76:79], v19 offset:8976
	v_cvt_pk_bf16_f32 v75, v73, s0
	global_store_short v[28:29], v75, off offset:1408
	s_waitcnt lgkmcnt(2)
	v_fma_f32 v75, v13, v6, v42
	v_fmac_f32_e32 v75, v10, v7
	ds_read_b128 v[80:83], v19 offset:10000
	v_fmac_f32_e32 v75, v2, v8
	s_waitcnt lgkmcnt(2)
	v_fma_f32 v84, v5, v14, v40
	v_fmac_f32_e32 v75, v3, v9
	v_fmac_f32_e32 v84, v11, v15
	ds_read_b128 v[6:9], v19 offset:8992
	s_waitcnt lgkmcnt(2)
	v_fmac_f32_e32 v75, v57, v76
	v_fmac_f32_e32 v84, v4, v16
	v_fmac_f32_e32 v75, v49, v77
	v_fmac_f32_e32 v84, v12, v17
	v_fmac_f32_e32 v75, v50, v78
	ds_read_b128 v[14:17], v19 offset:10016
	v_fmac_f32_e32 v75, v44, v79
	ds_read_b128 v[76:79], v19 offset:9008
	s_waitcnt lgkmcnt(3)
	v_fmac_f32_e32 v84, v51, v80
	v_fmac_f32_e32 v84, v56, v81
	v_fmac_f32_e32 v84, v54, v82
	s_waitcnt lgkmcnt(2)
	v_fmac_f32_e32 v75, v53, v6
	v_fmac_f32_e32 v84, v52, v83
	v_fmac_f32_e32 v75, v43, v7
	v_pk_mul_f32 v[6:7], v[30:31], v[8:9]
	ds_read_b128 v[80:83], v19 offset:10032
	s_waitcnt lgkmcnt(2)
	v_fmac_f32_e32 v84, v45, v14
	v_add_f32_e32 v6, v75, v6
	v_fmac_f32_e32 v84, v46, v15
	v_add_f32_e32 v8, v6, v7
	v_pk_mul_f32 v[6:7], v[34:35], v[16:17]
	s_nop 0
	v_add_f32_e32 v6, v84, v6
	v_add_f32_e32 v9, v6, v7
	s_waitcnt lgkmcnt(1)
	v_pk_mul_f32 v[6:7], v[32:33], v[76:77]
	s_nop 0
	v_add_f32_e32 v6, v8, v6
	v_add_f32_e32 v8, v6, v7
	s_waitcnt lgkmcnt(0)
	v_pk_mul_f32 v[6:7], v[22:23], v[80:81]
	s_nop 0
	v_add_f32_e32 v6, v9, v6
	v_add_f32_e32 v9, v6, v7
	v_pk_mul_f32 v[6:7], v[20:21], v[78:79]
	s_nop 0
	v_add_f32_e32 v6, v8, v6
	v_add_f32_e32 v8, v6, v7
	v_pk_mul_f32 v[6:7], v[24:25], v[82:83]
	s_nop 0
	v_add_f32_e32 v6, v9, v6
	v_add_f32_e32 v6, v6, v7
	v_med3_f32 v6, v6, s5, v38
	v_med3_f32 v7, v8, s5, v38
	v_mul_f32_e32 v6, 0x3fb8aa3b, v6
	v_mul_f32_e32 v7, 0x3fb8aa3b, v7
	v_exp_f32_e32 v75, v6
	v_exp_f32_e32 v76, v7
	ds_read_b128 v[6:9], v19 offset:9024
	ds_read_b128 v[14:17], v19 offset:10048
	ds_read_b128 v[78:81], v19 offset:9040
	v_cvt_pk_bf16_f32 v77, v75, s0
	global_store_short v[28:29], v77, off offset:1536
	s_waitcnt lgkmcnt(2)
	v_fma_f32 v77, v13, v6, v42
	v_fmac_f32_e32 v77, v10, v7
	ds_read_b128 v[82:85], v19 offset:10064
	v_fmac_f32_e32 v77, v2, v8
	s_waitcnt lgkmcnt(2)
	v_fma_f32 v86, v5, v14, v40
	v_fmac_f32_e32 v77, v3, v9
	v_fmac_f32_e32 v86, v11, v15
	ds_read_b128 v[6:9], v19 offset:9056
	s_waitcnt lgkmcnt(2)
	v_fmac_f32_e32 v77, v57, v78
	v_fmac_f32_e32 v86, v4, v16
	v_fmac_f32_e32 v77, v49, v79
	v_fmac_f32_e32 v86, v12, v17
	v_fmac_f32_e32 v77, v50, v80
	ds_read_b128 v[14:17], v19 offset:10080
	v_fmac_f32_e32 v77, v44, v81
	ds_read_b128 v[78:81], v19 offset:9072
	s_waitcnt lgkmcnt(3)
	v_fmac_f32_e32 v86, v51, v82
	v_fmac_f32_e32 v86, v56, v83
	v_fmac_f32_e32 v86, v54, v84
	s_waitcnt lgkmcnt(2)
	v_fmac_f32_e32 v77, v53, v6
	v_fmac_f32_e32 v86, v52, v85
	v_fmac_f32_e32 v77, v43, v7
	v_pk_mul_f32 v[6:7], v[30:31], v[8:9]
	ds_read_b128 v[82:85], v19 offset:10096
	s_waitcnt lgkmcnt(2)
	v_fmac_f32_e32 v86, v45, v14
	v_add_f32_e32 v6, v77, v6
	v_fmac_f32_e32 v86, v46, v15
	v_add_f32_e32 v8, v6, v7
	v_pk_mul_f32 v[6:7], v[34:35], v[16:17]
	s_nop 0
	v_add_f32_e32 v6, v86, v6
	v_add_f32_e32 v9, v6, v7
	s_waitcnt lgkmcnt(1)
	v_pk_mul_f32 v[6:7], v[32:33], v[78:79]
	s_nop 0
	v_add_f32_e32 v6, v8, v6
	v_add_f32_e32 v8, v6, v7
	s_waitcnt lgkmcnt(0)
	v_pk_mul_f32 v[6:7], v[22:23], v[82:83]
	s_nop 0
	v_add_f32_e32 v6, v9, v6
	v_add_f32_e32 v9, v6, v7
	v_pk_mul_f32 v[6:7], v[20:21], v[80:81]
	s_nop 0
	v_add_f32_e32 v6, v8, v6
	v_add_f32_e32 v8, v6, v7
	v_pk_mul_f32 v[6:7], v[24:25], v[84:85]
	s_nop 0
	v_add_f32_e32 v6, v9, v6
	v_add_f32_e32 v6, v6, v7
	v_med3_f32 v6, v6, s5, v38
	v_mul_f32_e32 v6, 0x3fb8aa3b, v6
	v_med3_f32 v7, v8, s5, v38
	v_exp_f32_e32 v77, v6
	v_mul_f32_e32 v6, 0x3fb8aa3b, v7
	v_exp_f32_e32 v78, v6
	ds_read_b128 v[6:9], v19 offset:9088
	v_cvt_pk_bf16_f32 v14, v77, s0
	global_store_short v[28:29], v14, off offset:1664
	ds_read_b128 v[14:17], v19 offset:9104
	ds_read_b128 v[80:83], v19 offset:10112
	s_waitcnt lgkmcnt(2)
	v_fma_f32 v79, v13, v6, v42
	v_fmac_f32_e32 v79, v10, v7
	v_fmac_f32_e32 v79, v2, v8
	v_fmac_f32_e32 v79, v3, v9
	ds_read_b128 v[6:9], v19 offset:10128
	s_waitcnt lgkmcnt(1)
	v_fma_f32 v86, v5, v80, v40
	v_fmac_f32_e32 v86, v11, v81
	v_fmac_f32_e32 v79, v57, v14
	v_fmac_f32_e32 v86, v4, v82
	v_fmac_f32_e32 v79, v49, v15
	v_fmac_f32_e32 v86, v12, v83
	v_fmac_f32_e32 v79, v50, v16
	v_fmac_f32_e32 v79, v44, v17
	ds_read_b128 v[14:17], v19 offset:9120
	s_waitcnt lgkmcnt(1)
	v_fmac_f32_e32 v86, v51, v6
	v_fmac_f32_e32 v86, v56, v7
	v_fmac_f32_e32 v86, v54, v8
	v_fmac_f32_e32 v86, v52, v9
	ds_read_b128 v[6:9], v19 offset:10144
	ds_read_b128 v[80:83], v19 offset:9136
	s_waitcnt lgkmcnt(2)
	v_fmac_f32_e32 v79, v53, v14
	v_fmac_f32_e32 v79, v43, v15
	v_pk_mul_f32 v[84:85], v[30:31], v[16:17]
	ds_read_b128 v[14:17], v19 offset:10160
	s_waitcnt lgkmcnt(2)
	v_fmac_f32_e32 v86, v45, v6
	v_add_f32_e32 v6, v79, v84
	v_fmac_f32_e32 v86, v46, v7
	v_add_f32_e32 v79, v6, v85
	v_pk_mul_f32 v[6:7], v[34:35], v[8:9]
	s_nop 0
	v_add_f32_e32 v6, v86, v6
	v_add_f32_e32 v8, v6, v7
	s_waitcnt lgkmcnt(1)
	v_pk_mul_f32 v[6:7], v[32:33], v[80:81]
	ds_read_b128 v[86:89], v19 offset:10176
	v_add_f32_e32 v6, v79, v6
	v_add_f32_e32 v9, v6, v7
	s_waitcnt lgkmcnt(1)
	v_pk_mul_f32 v[6:7], v[22:23], v[14:15]
	s_waitcnt lgkmcnt(0)
	v_fmac_f32_e32 v40, v5, v86
	v_add_f32_e32 v6, v8, v6
	v_add_f32_e32 v8, v6, v7
	v_pk_mul_f32 v[6:7], v[20:21], v[82:83]
	ds_read_b128 v[82:85], v19 offset:9152
	v_add_f32_e32 v6, v9, v6
	v_add_f32_e32 v9, v6, v7
	v_pk_mul_f32 v[6:7], v[24:25], v[16:17]
	ds_read_b128 v[14:17], v19 offset:10192
	v_add_f32_e32 v6, v8, v6
	v_add_f32_e32 v6, v6, v7
	v_med3_f32 v6, v6, s5, v38
	v_mul_f32_e32 v6, 0x3fb8aa3b, v6
	v_exp_f32_e32 v79, v6
	v_med3_f32 v7, v9, s5, v38
	v_mul_f32_e32 v7, 0x3fb8aa3b, v7
	v_exp_f32_e32 v80, v7
	v_cvt_pk_bf16_f32 v6, v79, s0
	global_store_short v[28:29], v6, off offset:1792
	ds_read_b128 v[6:9], v19 offset:9168
	s_waitcnt lgkmcnt(2)
	v_fmac_f32_e32 v42, v13, v82
	v_fmac_f32_e32 v42, v10, v83
	v_fmac_f32_e32 v40, v11, v87
	v_fmac_f32_e32 v42, v2, v84
	v_fmac_f32_e32 v42, v3, v85
	v_fmac_f32_e32 v40, v4, v88
	v_fmac_f32_e32 v40, v12, v89
	ds_read_b128 v[10:13], v19 offset:9184
	ds_read_b128 v[2:5], v19 offset:9200
	s_waitcnt lgkmcnt(2)
	v_fmac_f32_e32 v42, v57, v6
	v_fmac_f32_e32 v42, v49, v7
	ds_read_b128 v[82:85], v19 offset:10208
	v_fmac_f32_e32 v40, v51, v14
	v_fmac_f32_e32 v42, v50, v8
	v_fmac_f32_e32 v40, v56, v15
	v_fmac_f32_e32 v42, v44, v9
	v_fmac_f32_e32 v40, v54, v16
	s_waitcnt lgkmcnt(2)
	v_fmac_f32_e32 v42, v53, v10
	ds_read_b128 v[6:9], v19 offset:10224
	v_fmac_f32_e32 v40, v52, v17
	v_fmac_f32_e32 v42, v43, v11
	v_pk_mul_f32 v[10:11], v[30:31], v[12:13]
	s_waitcnt lgkmcnt(1)
	v_fmac_f32_e32 v40, v45, v82
	v_add_f32_e32 v10, v42, v10
	v_fmac_f32_e32 v40, v46, v83
	v_add_f32_e32 v12, v10, v11
	v_pk_mul_f32 v[10:11], v[34:35], v[84:85]
	v_pk_mul_f32 v[2:3], v[32:33], v[2:3]
	v_add_f32_e32 v10, v40, v10
	v_add_f32_e32 v2, v12, v2
	v_add_f32_e32 v10, v10, v11
	v_add_f32_e32 v11, v2, v3
	s_waitcnt lgkmcnt(0)
	v_pk_mul_f32 v[2:3], v[22:23], v[6:7]
	s_nop 0
	v_add_f32_e32 v2, v10, v2
	v_add_f32_e32 v6, v2, v3
	v_pk_mul_f32 v[2:3], v[20:21], v[4:5]
	v_cvt_pk_bf16_f32 v5, v64, v66
	v_add_f32_e32 v2, v11, v2
	v_add_f32_e32 v4, v2, v3
	v_pk_mul_f32 v[2:3], v[24:25], v[8:9]
	s_nop 0
	v_add_f32_e32 v2, v6, v2
	v_add_f32_e32 v2, v2, v3
	v_med3_f32 v2, v2, s5, v38
	v_mul_f32_e32 v2, 0x3fb8aa3b, v2
	v_exp_f32_e32 v10, v2
	v_med3_f32 v2, v4, s5, v38
	v_mul_f32_e32 v2, 0x3fb8aa3b, v2
	v_exp_f32_e32 v11, v2
	v_cvt_pk_bf16_f32 v2, v10, s0
	global_store_short v[28:29], v2, off offset:1920
	v_lshlrev_b32_e32 v2, 7, v36
	v_or3_b32 v26, v2, s4, v26
	v_lshl_add_u64 v[6:7], s[12:13], 0, v[26:27]
	v_cvt_pk_bf16_f32 v2, v37, v41
	v_cvt_pk_bf16_f32 v3, v48, v58
	v_cvt_pk_bf16_f32 v4, v60, v62
	global_store_dwordx4 v[6:7], v[2:5], off
	v_lshl_add_u64 v[8:9], s[14:15], 0, v[26:27]
	s_mov_b64 s[4:5], 0
	v_cvt_pk_bf16_f32 v2, v68, v70
	v_cvt_pk_bf16_f32 v3, v72, v74
	v_cvt_pk_bf16_f32 v4, v76, v78
	v_cvt_pk_bf16_f32 v5, v80, v11
	global_store_dwordx4 v[6:7], v[2:5], off offset:16
	s_nop 1
	v_cvt_pk_bf16_f32 v2, v18, v39
	v_cvt_pk_bf16_f32 v3, v47, v55
	v_cvt_pk_bf16_f32 v4, v59, v61
	v_cvt_pk_bf16_f32 v5, v63, v65
	global_store_dwordx4 v[8:9], v[2:5], off
	s_nop 1
	v_cvt_pk_bf16_f32 v2, v67, v69
	v_cvt_pk_bf16_f32 v3, v71, v73
	v_cvt_pk_bf16_f32 v4, v75, v77
	v_cvt_pk_bf16_f32 v5, v79, v10
	global_store_dwordx4 v[8:9], v[2:5], off offset:16
